# baseline (speedup 1.0000x reference)
_Z11attn_kernelPKDF16_S0_S0_PKjPf:
	s_and_b32 s27, s2, 7
	s_lshr_b32 s3, s2, 3
	s_lshr_b32 s12, s2, 6
	v_readfirstlane_b32 s23, v0
	s_mov_b32 s13, 0
	s_lshl_b32 s2, s2, 5
	s_load_dwordx8 s[4:11], s[0:1], 0x0
	s_and_b32 s28, s3, 0x1ffffff8
	s_lshr_b32 s20, s23, 6
	s_cmp_ge_u32 s20, 4
	s_cbranch_scc0 .Lattn_prio_done
	s_setprio 1
.Lattn_prio_done:
	s_lshl_b64 s[14:15], s[12:13], 11
	s_and_b32 s2, s2, 0x700
	s_or_b32 s16, s28, s27
	s_or_b32 s2, s14, s2
	s_lshl_b32 s3, s20, 5
	s_add_u32 s2, s2, s3
	s_addc_u32 s3, s15, 0
	s_lshl_b64 s[14:15], s[2:3], 10
	s_waitcnt lgkmcnt(0)
	s_add_u32 s4, s4, s14
	s_addc_u32 s5, s5, s15
	s_lshl_b32 s12, s27, 7
	s_add_u32 s4, s4, s12
	s_mov_b32 s17, s13
	s_addc_u32 s5, s5, 0
	s_lshl_b64 s[12:13], s[16:17], 18
	s_add_u32 s14, s6, s12
	s_addc_u32 s15, s7, s13
	s_add_u32 s12, s8, s12
	s_addc_u32 s13, s9, s13
	s_lshl_b32 s22, s20, 10
	s_cmp_lg_u32 0, -1
	v_and_b32_e32 v1, 63, v0
	s_cselect_b32 s6, 0, 0
	v_lshl_or_b32 v189, v1, 4, s22
	s_add_i32 s24, s22, s6
	s_mov_b32 s6, m0
	s_mov_b32 m0, s24
	s_nop 0
	global_load_lds_dwordx4 v189, s[14:15]
	s_mov_b32 m0, s6
	v_bfe_u32 v18, v0, 5, 1
	s_add_i32 s25, s24, 0x6000
	s_mov_b32 s6, m0
	s_mov_b32 m0, s25
	s_nop 0
	global_load_lds_dwordx4 v189, s[12:13]
	s_mov_b32 m0, s6
	v_and_b32_e32 v181, 31, v0
	s_add_u32 s6, s14, 0x2000
	v_lshlrev_b32_e32 v184, 4, v18
	s_addc_u32 s7, s15, 0
	s_add_i32 s17, s24, 0x2000
	s_mov_b32 s18, m0
	s_mov_b32 m0, s17
	s_nop 0
	global_load_lds_dwordx4 v189, s[6:7]
	s_mov_b32 m0, s18
	v_lshl_or_b32 v2, v181, 10, v184
	global_load_dwordx4 v[124:127], v2, s[4:5]
	global_load_dwordx4 v[120:123], v2, s[4:5] offset:32
	global_load_dwordx4 v[116:119], v2, s[4:5] offset:64
	global_load_dwordx4 v[112:115], v2, s[4:5] offset:96
	v_lshlrev_b32_e32 v182, 10, v18
	v_lshlrev_b32_e32 v19, 4, v181
	v_add3_u32 v190, 0, v182, v19
	s_lshl_b32 s5, s16, 2
	s_load_dword s5, s[10:11], s5 offset:0x0
	s_mov_b32 s4, 0x42a20000
	v_mov_b32_e32 v2, 0
	v_mov_b32_e32 v3, v2
	v_mov_b32_e32 v4, v2
	v_mov_b32_e32 v5, v2
	v_mov_b32_e32 v6, v2
	v_mov_b32_e32 v7, v2
	v_mov_b32_e32 v8, v2
	v_mov_b32_e32 v9, v2
	v_mov_b32_e32 v10, v2
	v_mov_b32_e32 v11, v2
	v_mov_b32_e32 v12, v2
	v_mov_b32_e32 v13, v2
	v_mov_b32_e32 v14, v2
	v_mov_b32_e32 v15, v2
	v_mov_b32_e32 v16, v2
	v_mov_b32_e32 v17, v2
	s_waitcnt vmcnt(3)
	v_fma_mix_f32 v19, v124, v124, 0 op_sel_hi:[1,1,0]
	s_nop 0
	v_fma_mix_f32 v19, v124, v124, v19 op_sel:[1,1,0] op_sel_hi:[1,1,0]
	s_nop 0
	v_fma_mix_f32 v19, v125, v125, v19 op_sel_hi:[1,1,0]
	s_nop 0
	v_fma_mix_f32 v19, v125, v125, v19 op_sel:[1,1,0] op_sel_hi:[1,1,0]
	s_nop 0
	v_fma_mix_f32 v19, v126, v126, v19 op_sel_hi:[1,1,0]
	s_nop 0
	v_fma_mix_f32 v19, v126, v126, v19 op_sel:[1,1,0] op_sel_hi:[1,1,0]
	s_nop 0
	v_fma_mix_f32 v19, v127, v127, v19 op_sel_hi:[1,1,0]
	s_nop 0
	v_fma_mix_f32 v19, v127, v127, v19 op_sel:[1,1,0] op_sel_hi:[1,1,0]
	s_waitcnt vmcnt(2)
	v_fma_mix_f32 v19, v120, v120, v19 op_sel_hi:[1,1,0]
	s_nop 0
	v_fma_mix_f32 v19, v120, v120, v19 op_sel:[1,1,0] op_sel_hi:[1,1,0]
	s_nop 0
	v_fma_mix_f32 v19, v121, v121, v19 op_sel_hi:[1,1,0]
	s_nop 0
	v_fma_mix_f32 v19, v121, v121, v19 op_sel:[1,1,0] op_sel_hi:[1,1,0]
	s_nop 0
	v_fma_mix_f32 v19, v122, v122, v19 op_sel_hi:[1,1,0]
	s_nop 0
	v_fma_mix_f32 v19, v122, v122, v19 op_sel:[1,1,0] op_sel_hi:[1,1,0]
	s_nop 0
	v_fma_mix_f32 v19, v123, v123, v19 op_sel_hi:[1,1,0]
	s_nop 0
	v_fma_mix_f32 v19, v123, v123, v19 op_sel:[1,1,0] op_sel_hi:[1,1,0]
	s_waitcnt vmcnt(1)
	v_fma_mix_f32 v19, v116, v116, v19 op_sel_hi:[1,1,0]
	s_nop 0
	v_fma_mix_f32 v19, v116, v116, v19 op_sel:[1,1,0] op_sel_hi:[1,1,0]
	s_nop 0
	v_fma_mix_f32 v19, v117, v117, v19 op_sel_hi:[1,1,0]
	s_nop 0
	v_fma_mix_f32 v19, v117, v117, v19 op_sel:[1,1,0] op_sel_hi:[1,1,0]
	s_nop 0
	v_fma_mix_f32 v19, v118, v118, v19 op_sel_hi:[1,1,0]
	s_nop 0
	v_fma_mix_f32 v19, v118, v118, v19 op_sel:[1,1,0] op_sel_hi:[1,1,0]
	s_nop 0
	v_fma_mix_f32 v19, v119, v119, v19 op_sel_hi:[1,1,0]
	s_nop 0
	v_fma_mix_f32 v19, v119, v119, v19 op_sel:[1,1,0] op_sel_hi:[1,1,0]
	s_waitcnt vmcnt(0)
	v_fma_mix_f32 v19, v112, v112, v19 op_sel_hi:[1,1,0]
	s_nop 0
	v_fma_mix_f32 v19, v112, v112, v19 op_sel:[1,1,0] op_sel_hi:[1,1,0]
	s_nop 0
	v_fma_mix_f32 v19, v113, v113, v19 op_sel_hi:[1,1,0]
	s_nop 0
	v_fma_mix_f32 v19, v113, v113, v19 op_sel:[1,1,0] op_sel_hi:[1,1,0]
	s_nop 0
	v_fma_mix_f32 v19, v114, v114, v19 op_sel_hi:[1,1,0]
	s_nop 0
	v_fma_mix_f32 v19, v114, v114, v19 op_sel:[1,1,0] op_sel_hi:[1,1,0]
	s_nop 0
	v_fma_mix_f32 v19, v115, v115, v19 op_sel_hi:[1,1,0]
	s_nop 0
	v_fma_mix_f32 v19, v115, v115, v19 op_sel:[1,1,0] op_sel_hi:[1,1,0]
	s_nop 0
	v_mov_b32_e32 v20, v19
	s_nop 1
	v_permlane32_swap_b32_e32 v19, v20
	v_add_f32_e32 v19, v19, v20
	s_waitcnt lgkmcnt(0)
	v_mul_f32_e32 v19, s5, v19
	v_cmp_ge_f32_e32 vcc, s4, v19
	s_cmp_eq_u64 vcc, exec
	s_cselect_b64 s[4:5], -1, 0
	s_add_u32 s6, s14, 0x4000
	s_addc_u32 s7, s15, 0
	s_add_i32 s10, s24, 0x4000
	s_mov_b32 s11, m0
	s_mov_b32 m0, s10
	s_nop 0
	global_load_lds_dwordx4 v189, s[6:7]
	s_mov_b32 m0, s11
	s_waitcnt vmcnt(3) lgkmcnt(0)
	s_barrier
	ds_read_b128 v[20:23], v190
	ds_read_b128 v[24:27], v190 offset:512
	s_waitcnt lgkmcnt(1)
	v_mfma_f32_32x32x16_f16 v[96:111], v[20:23], v[124:127], v[2:17]
	v_cndmask_b32_e64 v19, 0, 1, s[4:5]
	s_nop 0
	v_readfirstlane_b32 s4, v19
	s_bitcmp1_b32 s4, 0
	s_cselect_b64 s[16:17], -1, 0
	s_xor_b64 s[18:19], s[16:17], -1
	s_mov_b64 s[4:5], -1
	s_waitcnt lgkmcnt(0)
	v_mfma_f32_32x32x16_f16 v[80:95], v[24:27], v[124:127], v[2:17]
	ds_read_b128 v[20:23], v190 offset:2048
	ds_read_b128 v[24:27], v190 offset:2560
	s_and_b64 vcc, exec, s[18:19]
	s_waitcnt lgkmcnt(1)
	v_mfma_f32_32x32x16_f16 v[96:111], v[20:23], v[120:123], v[96:111]
	s_waitcnt lgkmcnt(0)
	v_mfma_f32_32x32x16_f16 v[80:95], v[24:27], v[120:123], v[80:95]
	ds_read_b128 v[20:23], v190 offset:4096
	ds_read_b128 v[24:27], v190 offset:4608
	s_waitcnt lgkmcnt(1)
	v_mfma_f32_32x32x16_f16 v[96:111], v[20:23], v[116:119], v[96:111]
	s_waitcnt lgkmcnt(0)
	v_mfma_f32_32x32x16_f16 v[80:95], v[24:27], v[116:119], v[80:95]
	ds_read_b128 v[20:23], v190 offset:6144
	ds_read_b128 v[24:27], v190 offset:6656
	s_waitcnt lgkmcnt(1)
	v_mfma_f32_32x32x16_f16 v[96:111], v[20:23], v[112:115], v[96:111]
	s_waitcnt lgkmcnt(0)
	v_mfma_f32_32x32x16_f16 v[80:95], v[24:27], v[112:115], v[80:95]
	s_cbranch_vccz .LBB2_2
	v_max3_f32 v19, v96, v97, v80
	v_max3_f32 v20, v98, v99, v81
	s_nop 0
	v_max3_f32 v19, v19, v82, v83
	v_max3_f32 v20, v20, v102, v103
	s_nop 0
	v_max3_f32 v19, v19, v100, v101
	v_max3_f32 v20, v20, v86, v87
	s_nop 0
	v_max3_f32 v19, v19, v84, v85
	v_max3_f32 v20, v20, v106, v107
	s_nop 0
	v_max3_f32 v19, v19, v104, v105
	v_max3_f32 v20, v20, v90, v91
	s_nop 0
	v_max3_f32 v19, v19, v88, v89
	v_max3_f32 v20, v20, v110, v111
	s_nop 0
	v_max3_f32 v19, v19, v108, v109
	v_max3_f32 v20, v20, v94, v95
	s_nop 0
	v_max3_f32 v19, v19, v92, v93
	s_nop 0
	v_max_f32 v19, v19, v20
	s_nop 0
	v_mov_b32_e32 v20, v19
	s_nop 1
	v_permlane32_swap_b32_e32 v19, v20
	v_max_f32 v180, v19, v20
	s_nop 0
	v_sub_f32_e32 v19, v96, v180
	v_exp_f32_e32 v64, v19
	v_sub_f32_e32 v19, v80, v180
	v_exp_f32_e32 v48, v19
	v_sub_f32_e32 v19, v97, v180
	v_exp_f32_e32 v65, v19
	v_sub_f32_e32 v19, v81, v180
	v_exp_f32_e32 v49, v19
	v_sub_f32_e32 v19, v98, v180
	v_exp_f32_e32 v66, v19
	v_sub_f32_e32 v19, v82, v180
	v_exp_f32_e32 v50, v19
	v_sub_f32_e32 v19, v99, v180
	v_exp_f32_e32 v67, v19
	v_sub_f32_e32 v19, v83, v180
	v_exp_f32_e32 v51, v19
	v_sub_f32_e32 v19, v100, v180
	v_exp_f32_e32 v68, v19
	v_sub_f32_e32 v19, v84, v180
	v_exp_f32_e32 v52, v19
	v_sub_f32_e32 v19, v101, v180
	v_exp_f32_e32 v69, v19
	v_sub_f32_e32 v19, v85, v180
	v_exp_f32_e32 v53, v19
	v_sub_f32_e32 v19, v102, v180
	v_exp_f32_e32 v70, v19
	v_sub_f32_e32 v19, v86, v180
	v_exp_f32_e32 v54, v19
	v_sub_f32_e32 v19, v103, v180
	v_exp_f32_e32 v71, v19
	v_sub_f32_e32 v19, v87, v180
	v_exp_f32_e32 v55, v19
	v_sub_f32_e32 v19, v104, v180
	v_exp_f32_e32 v72, v19
	v_sub_f32_e32 v19, v105, v180
	v_exp_f32_e32 v73, v19
	v_sub_f32_e32 v19, v106, v180
	v_exp_f32_e32 v74, v19
	v_sub_f32_e32 v19, v107, v180
	v_exp_f32_e32 v75, v19
	v_sub_f32_e32 v19, v108, v180
	v_exp_f32_e32 v76, v19
	v_sub_f32_e32 v19, v109, v180
	v_exp_f32_e32 v77, v19
	v_sub_f32_e32 v19, v110, v180
	v_xor_b32_e32 v32, 0x80000000, v180
	v_exp_f32_e32 v78, v19
	v_sub_f32_e32 v19, v111, v180
	v_mov_b32_e32 v33, v32
	v_mov_b32_e32 v34, v32
	v_mov_b32_e32 v35, v32
	v_mov_b32_e32 v36, v32
	v_mov_b32_e32 v37, v32
	v_mov_b32_e32 v38, v32
	v_mov_b32_e32 v39, v32
	v_mov_b32_e32 v40, v32
	v_mov_b32_e32 v41, v32
	v_mov_b32_e32 v42, v32
	v_mov_b32_e32 v43, v32
	v_mov_b32_e32 v44, v32
	v_mov_b32_e32 v45, v32
	v_mov_b32_e32 v46, v32
	v_mov_b32_e32 v47, v32
	v_pk_add_f32 v[56:57], v[88:89], v[180:181] op_sel_hi:[1,0] neg_lo:[0,1] neg_hi:[0,1]
	v_pk_add_f32 v[58:59], v[90:91], v[180:181] op_sel_hi:[1,0] neg_lo:[0,1] neg_hi:[0,1]
	v_pk_add_f32 v[60:61], v[92:93], v[180:181] op_sel_hi:[1,0] neg_lo:[0,1] neg_hi:[0,1]
	v_exp_f32_e32 v79, v19
	v_pk_add_f32 v[62:63], v[94:95], v[180:181] op_sel_hi:[1,0] neg_lo:[0,1] neg_hi:[0,1]
	s_load_dwordx2 s[6:7], s[0:1], 0x20
	s_lshl_b32 s21, s27, 6
	s_cbranch_execz .LBB2_3
	s_branch .LBB2_4

.LBB2_4:
	s_and_b32 s0, s23, 0x3fffffc0
	s_lshl_b32 s0, s0, 2
	s_lshl_b64 s[10:11], s[2:3], 9
	s_add_i32 s23, s0, 0
	s_add_u32 s0, s14, 0x6000
	s_waitcnt vmcnt(0) lgkmcnt(0)
	s_barrier
	s_addc_u32 s1, s15, 0
	s_mov_b32 s2, m0
	s_mov_b32 m0, s24
	s_nop 0
	global_load_lds_dwordx4 v189, s[0:1]
	s_mov_b32 m0, s2
	s_add_u32 s0, s12, 0x2000
	s_addc_u32 s1, s13, 0
	s_cmp_lg_u32 0, -1
	s_cselect_b32 s2, 0, 0
	s_add_i32 s2, s2, s22
	s_add_i32 s2, s2, 0x8000
	s_mov_b32 s4, m0
	s_mov_b32 m0, s2
	s_nop 0
	global_load_lds_dwordx4 v189, s[0:1]
	s_mov_b32 m0, s4
	ds_read_b128 v[172:175], v190 offset:8192
	ds_read_b128 v[168:171], v190 offset:8704
	ds_read_b128 v[164:167], v190 offset:10240
	ds_read_b128 v[160:163], v190 offset:10752
	ds_read_b128 v[156:159], v190 offset:12288
	ds_read_b128 v[152:155], v190 offset:12800
	ds_read_b128 v[148:151], v190 offset:14336
	ds_read_b128 v[144:147], v190 offset:14848
	s_mov_b32 s3, 0
	s_add_i32 s2, s28, s27
	s_lshl_b64 s[4:5], s[2:3], 18
	v_lshlrev_b32_e32 v2, 1, v1
	v_lshlrev_b32_e32 v3, 3, v0
	s_add_u32 s2, s8, s4
	v_and_b32_e32 v2, 32, v2
	v_and_b32_e32 v3, 24, v3
	v_lshlrev_b32_e32 v185, 4, v0
	s_waitcnt vmcnt(2) lgkmcnt(0)
	s_barrier
	s_addc_u32 s4, s9, s5
	v_add3_u32 v2, 0, v2, v3
	v_lshlrev_b32_e32 v3, 8, v18
	v_and_b32_e32 v0, 0xc0, v185
	s_add_u32 s27, s2, 0x2000
	v_mov_b32_e32 v188, 0
	v_mov_b32_e32 v192, 0
	v_lshrrev_b32_e32 v183, 4, v1
	v_add3_u32 v187, v2, v3, v0
	s_mov_b32 s26, -1
	v_cmp_gt_u32_e64 s[0:1], 32, v1
	v_lshl_add_u32 v186, v181, 2, s23
	s_addc_u32 s28, s4, 0
	s_movk_i32 s29, 0x4000
	s_movk_i32 s31, 0x2000
	s_mov_b64 s[8:9], 0
	s_mov_b32 s30, 0x41000000
	v_mov_b32_e32 v0, 0
	v_mov_b32_e32 v1, v188
	v_mov_b32_e32 v2, v188
	v_mov_b32_e32 v3, v188
	v_mov_b32_e32 v4, v188
	v_mov_b32_e32 v5, v188
	v_mov_b32_e32 v6, v188
	v_mov_b32_e32 v7, v188
	v_mov_b32_e32 v8, v188
	v_mov_b32_e32 v9, v188
	v_mov_b32_e32 v10, v188
	v_mov_b32_e32 v11, v188
	v_mov_b32_e32 v12, v188
	v_mov_b32_e32 v13, v188
	v_mov_b32_e32 v14, v188
	v_mov_b32_e32 v15, v188
	v_mov_b32_e32 v16, 0
	v_mov_b32_e32 v17, v188
	v_mov_b32_e32 v18, v188
	v_mov_b32_e32 v19, v188
	v_mov_b32_e32 v20, v188
	v_mov_b32_e32 v21, v188
	v_mov_b32_e32 v22, v188
	v_mov_b32_e32 v23, v188
	v_mov_b32_e32 v24, v188
	v_mov_b32_e32 v25, v188
	v_mov_b32_e32 v26, v188
	v_mov_b32_e32 v27, v188
	v_mov_b32_e32 v28, v188
	v_mov_b32_e32 v29, v188
	v_mov_b32_e32 v30, v188
	v_mov_b32_e32 v31, v188
.LBB2_5:
	s_add_i32 s26, s26, 2
	v_add_u32_e32 v191, s3, v187
	ds_read_b64_tr_b16 v[176:177], v191 offset:24576
	ds_read_b64_tr_b16 v[178:179], v191 offset:25088
	v_mfma_f32_32x32x16_f16 v[96:111], v[172:175], v[124:127], v[32:47]
	v_exp_f32_e32 v56, v56
	v_exp_f32_e32 v57, v57
	v_cvt_pk_f16_f32 v140, v64, v65
	v_cvt_pk_f16_f32 v141, v66, v67
	ds_read_b64_tr_b16 v[172:173], v191 offset:28672
	ds_read_b64_tr_b16 v[174:175], v191 offset:29184
	v_mfma_f32_32x32x16_f16 v[80:95], v[168:171], v[124:127], v[32:47]
	v_exp_f32_e32 v58, v58
	v_exp_f32_e32 v59, v59
	v_pk_add_f16 v128, v140, v141
	v_cvt_pk_f16_f32 v142, v68, v69
	v_cvt_pk_f16_f32 v143, v70, v71
	ds_read_b64_tr_b16 v[64:65], v191 offset:25600
	ds_read_b64_tr_b16 v[66:67], v191 offset:26112
	v_mfma_f32_32x32x16_f16 v[96:111], v[164:167], v[120:123], v[96:111]
	v_exp_f32_e32 v60, v60
	v_exp_f32_e32 v61, v61
	v_pk_add_f16 v129, v142, v143
	v_cvt_pk_f16_f32 v136, v72, v73
	v_cvt_pk_f16_f32 v137, v74, v75
	ds_read_b64_tr_b16 v[68:69], v191 offset:29696
	ds_read_b64_tr_b16 v[70:71], v191 offset:30208
	v_mfma_f32_32x32x16_f16 v[80:95], v[160:163], v[120:123], v[80:95]
	v_exp_f32_e32 v62, v62
	v_exp_f32_e32 v63, v63
	v_pk_add_f16 v72, v136, v137
	v_pk_add_f16 v128, v128, v129
	v_cvt_pk_f16_f32 v138, v76, v77
	v_cvt_pk_f16_f32 v139, v78, v79
	s_min_u32 s2, s26, 28
	s_lshl_b32 s2, s2, 13
	s_add_u32 s2, s14, s2
	s_addc_u32 s3, s15, 0
	s_add_u32 s2, s2, 0x6000
	s_addc_u32 s3, s3, 0
	s_add_i32 s4, s31, s24
	s_mov_b32 s5, m0
	s_mov_b32 m0, s4
	s_nop 0
	global_load_lds_dwordx4 v189, s[2:3]
	s_mov_b32 m0, s5
	ds_read_b64_tr_b16 v[76:77], v191 offset:26624
	ds_read_b64_tr_b16 v[78:79], v191 offset:27136
	v_mfma_f32_32x32x16_f16 v[96:111], v[156:159], v[116:119], v[96:111]
	v_pk_add_f16 v73, v138, v139
	v_cvt_pk_f16_f32 v132, v48, v49
	v_cvt_pk_f16_f32 v133, v50, v51
	ds_read_b64_tr_b16 v[48:49], v191 offset:30720
	ds_read_b64_tr_b16 v[50:51], v191 offset:31232
	v_mfma_f32_32x32x16_f16 v[80:95], v[152:155], v[116:119], v[80:95]
	v_pk_add_f16 v129, v72, v73
	v_cvt_pk_f16_f32 v134, v52, v53
	v_cvt_pk_f16_f32 v135, v54, v55
	v_pk_add_f16 v156, v132, v133
	s_add_u32 s2, s27, 0x2000
	s_addc_u32 s3, s28, 0
	s_add_i32 s4, s29, s25
	s_mov_b32 s5, m0
	s_mov_b32 m0, s4
	s_nop 0
	global_load_lds_dwordx4 v189, s[2:3]
	s_mov_b32 m0, s5
	ds_read_b64_tr_b16 v[72:73], v191 offset:27648
	ds_read_b64_tr_b16 v[74:75], v191 offset:28160
	v_mfma_f32_32x32x16_f16 v[96:111], v[148:151], v[112:115], v[96:111]
	v_pk_add_f16 v153, v128, v129
	v_cvt_pk_f16_f32 v128, v56, v57
	v_cvt_pk_f16_f32 v129, v58, v59
	v_pk_add_f16 v152, v134, v135
	ds_read_b64_tr_b16 v[52:53], v191 offset:31744
	ds_read_b64_tr_b16 v[54:55], v191 offset:32256
	v_mfma_f32_32x32x16_f16 v[80:95], v[144:147], v[112:115], v[80:95]
	v_pk_add_f16 v56, v128, v129
	v_pk_add_f16 v57, v156, v152
	v_cvt_pk_f16_f32 v130, v60, v61
	v_cvt_pk_f16_f32 v131, v62, v63
	s_andn2_b64 vcc, exec, s[18:19]
	v_pk_add_f16 v57, v153, v57
	v_pk_add_f16 v58, v130, v131
	s_cbranch_vccnz .LBB2_7
	v_pk_add_f16 v59, v56, v58
	v_max3_f32 v61, v96, v97, v80
	v_max3_f32 v62, v98, v99, v81
	s_mov_b64 s[8:9], 0
	v_pk_add_f16 v59, v57, v59
	s_nop 0
	v_cvt_f32_f16_e32 v60, v59
	v_cvt_f32_f16_sdwa v59, v59 dst_sel:DWORD dst_unused:UNUSED_PAD src0_sel:WORD_1
	v_add_f32_e32 v59, v59, v60
	v_add_f32_e32 v188, v188, v59
	v_max3_f32 v59, v61, v82, v83
	v_max3_f32 v60, v62, v102, v103
	s_nop 0
	v_max3_f32 v59, v59, v100, v101
	v_max3_f32 v60, v60, v86, v87
	s_nop 0
	v_max3_f32 v59, v59, v84, v85
	v_max3_f32 v60, v60, v106, v107
	s_nop 0
	v_max3_f32 v59, v59, v104, v105
	v_max3_f32 v60, v60, v90, v91
	s_nop 0
	v_max3_f32 v59, v59, v88, v89
	v_max3_f32 v60, v60, v110, v111
	s_nop 0
	v_max3_f32 v59, v59, v108, v109
	v_max3_f32 v60, v60, v94, v95
	s_nop 0
	v_max3_f32 v59, v59, v92, v93
	s_nop 0
	v_max_f32 v59, v59, v60
	s_nop 0
	v_mov_b32_e32 v60, v59
	s_nop 1
	v_permlane32_swap_b32_e32 v59, v60
	v_max_f32 v59, v59, v60
	s_nop 0
	v_cmp_lt_f32_e32 vcc, s30, v59
	s_cbranch_vccnz .LBB2_19
